# speedup vs baseline: 1.0391x; 1.0010x over previous
.Lp1_fin:
	s_lshl_b64 s[0:1], s[20:21], 1
	s_add_u32 s0, s18, s0
	s_addc_u32 s1, s19, s1
	global_load_dwordx4 v[2:5], v[66:67], off
	global_load_dwordx4 v[6:9], v[68:69], off
	v_lshlrev_b32_e32 v10, 1, v79
	global_load_dwordx4 v[10:13], v10, s[0:1]
	v_lshlrev_b32_e32 v14, 1, v80
	global_load_dwordx4 v[14:17], v14, s[0:1]
	v_mov_b32_e32 v200, 0
	v_mov_b32_e32 v201, 0
	v_mov_b32_e32 v202, 0
	v_mov_b32_e32 v83, 0
	v_exp_f32_e32 v34, v34
	v_exp_f32_e32 v35, v35
	v_add_f32_e32 v200, v200, v34
	v_exp_f32_e32 v36, v36
	v_add_f32_e32 v201, v201, v35
	v_exp_f32_e32 v37, v37
	v_add_f32_e32 v202, v202, v36
	v_exp_f32_e32 v38, v38
	v_add_f32_e32 v83, v83, v37
	v_exp_f32_e32 v39, v39
	v_add_f32_e32 v200, v200, v38
	v_exp_f32_e32 v40, v40
	v_add_f32_e32 v201, v201, v39
	v_exp_f32_e32 v41, v41
	v_add_f32_e32 v202, v202, v40
	v_exp_f32_e32 v42, v42
	v_add_f32_e32 v83, v83, v41
	v_exp_f32_e32 v43, v43
	v_add_f32_e32 v200, v200, v42
	v_exp_f32_e32 v44, v44
	v_add_f32_e32 v201, v201, v43
	v_exp_f32_e32 v45, v45
	v_add_f32_e32 v202, v202, v44
	v_exp_f32_e32 v46, v46
	v_add_f32_e32 v83, v83, v45
	v_exp_f32_e32 v47, v47
	v_add_f32_e32 v200, v200, v46
	v_exp_f32_e32 v48, v48
	v_add_f32_e32 v201, v201, v47
	v_exp_f32_e32 v49, v49
	v_add_f32_e32 v202, v202, v48
	v_exp_f32_e32 v50, v50
	v_add_f32_e32 v83, v83, v49
	v_exp_f32_e32 v51, v51
	v_add_f32_e32 v200, v200, v50
	v_exp_f32_e32 v52, v52
	v_add_f32_e32 v201, v201, v51
	v_exp_f32_e32 v53, v53
	v_add_f32_e32 v202, v202, v52
	v_exp_f32_e32 v54, v54
	v_add_f32_e32 v83, v83, v53
	v_exp_f32_e32 v55, v55
	v_add_f32_e32 v200, v200, v54
	v_exp_f32_e32 v56, v56
	v_add_f32_e32 v201, v201, v55
	v_exp_f32_e32 v57, v57
	v_add_f32_e32 v202, v202, v56
	v_exp_f32_e32 v58, v58
	v_add_f32_e32 v83, v83, v57
	v_exp_f32_e32 v59, v59
	v_add_f32_e32 v200, v200, v58
	v_exp_f32_e32 v60, v60
	v_add_f32_e32 v201, v201, v59
	v_exp_f32_e32 v61, v61
	v_add_f32_e32 v202, v202, v60
	v_exp_f32_e32 v62, v62
	v_add_f32_e32 v83, v83, v61
	v_exp_f32_e32 v63, v63
	v_add_f32_e32 v200, v200, v62
	v_exp_f32_e32 v64, v64
	v_add_f32_e32 v201, v201, v63
	v_exp_f32_e32 v65, v65
	v_add_f32_e32 v202, v202, v64
	v_add_f32_e32 v83, v83, v65
	v_add_f32_e32 v200, v200, v201
	v_add_f32_e32 v202, v202, v83
	v_add_f32_e32 v200, v200, v202
	v_add_f32_e32 v82, v82, v200
	s_barrier
	v_mbcnt_lo_u32_b32 v21, -1, 0
	v_mbcnt_hi_u32_b32 v21, -1, v21
	v_and_b32_e32 v23, 64, v21
	v_xor_b32_e32 v22, 32, v21
	v_add_u32_e32 v24, 64, v23
	v_cmp_lt_i32_e32 vcc, v22, v24
	v_cndmask_b32_e32 v21, v21, v22, vcc
	v_lshlrev_b32_e32 v21, 2, v21
	ds_bpermute_b32 v22, v21, v81
	v_mov_b32_e32 v18, v82
	ds_bpermute_b32 v19, v21, v18
	v_max_f32_e32 v21, v81, v81
	s_mov_b32 s15, 0
	s_waitcnt lgkmcnt(1)
	v_max_f32_e32 v20, v22, v22
	v_max_f32_e32 v20, v21, v20
	v_sub_f32_e32 v22, v22, v20
	v_sub_f32_e32 v21, v81, v20
	v_exp_f32_e32 v22, v22
	v_exp_f32_e32 v21, v21
	s_lshl_b64 s[18:19], s[14:15], 18
	v_mov_b32_e32 v131, 0
	s_waitcnt lgkmcnt(0)
	v_mul_f32_e32 v19, v22, v19
	v_fmac_f32_e32 v19, v18, v21
	v_div_scale_f32 v18, s[10:11], v19, v19, 1.0
	s_movk_i32 s10, 0x60
	s_nop 0
	v_mad_u32_u24 v188, v73, s10, v74
	v_mad_u32_u24 v189, v75, s10, v74
	s_waitcnt vmcnt(3)
	ds_write_b128 v77, v[2:5]
	s_waitcnt vmcnt(2)
	ds_write_b128 v78, v[6:9]
	v_lshlrev_b32_e32 v2, 1, v188
	s_waitcnt vmcnt(1)
	ds_write_b128 v2, v[10:13]
	v_lshlrev_b32_e32 v2, 1, v189
	s_mul_i32 s10, s14, 0x1200
	s_waitcnt vmcnt(0)
	ds_write_b128 v2, v[14:17]
	s_add_i32 s10, s10, 0xa800
	v_lshrrev_b32_e32 v2, 2, v0
	v_and_or_b32 v3, v2, 3, v1
	s_movk_i32 s11, 0x48
	v_mov_b32_e32 v5, s10
	v_add_u32_e32 v4, s10, v76
	v_mad_u32_u24 v5, v3, s11, v5
	s_lshl_b64 s[10:11], s[12:13], 24
	s_and_b32 s13, s2, 15
	s_lshl_b32 s13, s13, 20
	v_and_b32_e32 v0, 3, v0
	s_or_b32 s10, s10, s13
	v_and_or_b32 v0, v2, 4, v0
	s_add_u32 s10, s10, s18
	v_lshlrev_b32_e32 v0, 3, v0
	v_mul_u32_u24_e32 v2, 0xc0, v3
	v_lshlrev_b32_e32 v3, 13, v72
	s_addc_u32 s11, s11, s19
	v_or_b32_e32 v185, v2, v0
	v_or_b32_e32 v2, v3, v164
	s_add_u32 s10, s4, s10
	v_lshlrev_b32_e32 v130, 2, v2
	s_addc_u32 s11, s5, s11
	v_lshl_add_u64 v[2:3], s[10:11], 0, v[130:131]
	s_mov_b64 s[18:19], 0x80
	v_lshl_add_u64 v[132:133], v[2:3], 0, s[18:19]
	v_or_b32_e32 v2, 0x36000, v130
	v_mov_b32_e32 v3, v131
	v_lshl_add_u64 v[134:135], s[10:11], 0, v[2:3]
	v_or_b32_e32 v2, 0x2000, v130
	v_lshl_add_u64 v[2:3], s[10:11], 0, v[2:3]
	v_lshl_add_u64 v[136:137], v[2:3], 0, s[18:19]
	v_or_b32_e32 v2, 0x34000, v130
	v_mov_b32_e32 v3, v131
	v_rcp_f32_e32 v21, v18
	v_lshl_add_u64 v[138:139], s[10:11], 0, v[2:3]
	v_or_b32_e32 v2, 0x4000, v130
	v_lshl_add_u64 v[2:3], s[10:11], 0, v[2:3]
	v_lshl_add_u64 v[140:141], v[2:3], 0, s[18:19]
	v_or_b32_e32 v2, 0x32000, v130
	v_mov_b32_e32 v3, v131
	v_lshl_add_u64 v[142:143], s[10:11], 0, v[2:3]
	v_or_b32_e32 v2, 0x6000, v130
	v_fma_f32 v22, -v18, v21, 1.0
	v_lshl_add_u64 v[2:3], s[10:11], 0, v[2:3]
	v_fmac_f32_e32 v21, v22, v21
	v_div_scale_f32 v22, vcc, 1.0, v19, 1.0
	v_lshl_add_u64 v[144:145], v[2:3], 0, s[18:19]
	v_or_b32_e32 v2, 0x30000, v130
	v_mov_b32_e32 v3, v131
	v_mul_f32_e32 v24, v22, v21
	v_lshl_add_u64 v[146:147], s[10:11], 0, v[2:3]
	v_or_b32_e32 v2, 0x10000, v130
	v_fma_f32 v25, -v18, v24, v22
	v_lshl_add_u64 v[2:3], s[10:11], 0, v[2:3]
	v_fmac_f32_e32 v24, v25, v21
	v_lshl_add_u64 v[148:149], v[2:3], 0, s[18:19]
	v_or_b32_e32 v2, 0x26000, v130
	v_mov_b32_e32 v3, v131
	v_fma_f32 v18, -v18, v24, v22
	v_lshl_add_u64 v[150:151], s[10:11], 0, v[2:3]
	v_or_b32_e32 v2, 0x12000, v130
	v_div_fmas_f32 v18, v18, v21, v24
	v_lshlrev_b32_e32 v184, 2, v72
	v_lshl_add_u64 v[2:3], s[10:11], 0, v[2:3]
	v_div_fixup_f32 v18, v18, v19, 1.0
	v_or_b32_e32 v19, v184, v23
	v_lshl_add_u64 v[152:153], v[2:3], 0, s[18:19]
	v_or_b32_e32 v2, 0x24000, v130
	v_mov_b32_e32 v3, v131
	v_lshlrev_b32_e32 v19, 2, v19
	v_lshl_add_u64 v[154:155], s[10:11], 0, v[2:3]
	v_or_b32_e32 v2, 0x14000, v130
	ds_bpermute_b32 v33, v19, v20 offset:36
	ds_bpermute_b32 v32, v19, v20 offset:40
	ds_bpermute_b32 v35, v19, v20 offset:44
	ds_bpermute_b32 v34, v19, v20 offset:64
	ds_bpermute_b32 v37, v19, v20 offset:68
	ds_bpermute_b32 v36, v19, v20 offset:72
	ds_bpermute_b32 v39, v19, v20 offset:76
	ds_bpermute_b32 v38, v19, v20 offset:96
	ds_bpermute_b32 v41, v19, v20 offset:100
	ds_bpermute_b32 v40, v19, v20 offset:104
	ds_bpermute_b32 v43, v19, v20 offset:108
	v_lshl_add_u64 v[2:3], s[10:11], 0, v[2:3]
	ds_bpermute_b32 v46, v19, v20 offset:32
	ds_bpermute_b32 v47, v19, v20 offset:12
	ds_bpermute_b32 v42, v19, v20 offset:8
	ds_bpermute_b32 v45, v19, v20 offset:4
	ds_bpermute_b32 v44, v19, v20
	ds_bpermute_b32 v183, v19, v18
	ds_bpermute_b32 v182, v19, v18 offset:4
	ds_bpermute_b32 v181, v19, v18 offset:8
	ds_bpermute_b32 v180, v19, v18 offset:12
	ds_bpermute_b32 v179, v19, v18 offset:32
	ds_bpermute_b32 v178, v19, v18 offset:36
	ds_bpermute_b32 v177, v19, v18 offset:40
	ds_bpermute_b32 v176, v19, v18 offset:44
	ds_bpermute_b32 v175, v19, v18 offset:64
	ds_bpermute_b32 v174, v19, v18 offset:68
	ds_bpermute_b32 v173, v19, v18 offset:72
	ds_bpermute_b32 v172, v19, v18 offset:76
	ds_bpermute_b32 v171, v19, v18 offset:96
	ds_bpermute_b32 v170, v19, v18 offset:100
	ds_bpermute_b32 v169, v19, v18 offset:104
	ds_bpermute_b32 v168, v19, v18 offset:108
	v_lshl_add_u64 v[156:157], v[2:3], 0, s[18:19]
	v_or_b32_e32 v2, 0x22000, v130
	v_mov_b32_e32 v3, v131
	v_lshl_add_u64 v[158:159], s[10:11], 0, v[2:3]
	v_or_b32_e32 v2, 0x16000, v130
	v_lshl_add_u64 v[2:3], s[10:11], 0, v[2:3]
	v_lshl_add_u64 v[160:161], v[2:3], 0, s[18:19]
	v_or_b32_e32 v2, 0x20000, v130
	v_mov_b32_e32 v3, v131
	v_add_u32_e32 v187, v4, v1
	v_lshl_add_u64 v[162:163], s[10:11], 0, v[2:3]
	s_mov_b64 s[42:43], s[10:11]
	s_mov_b64 s[10:11], 0
	s_movk_i32 s13, 0x3000
	s_waitcnt lgkmcnt(14)
	v_xor_b32_e32 v63, 0x80000000, v43
	v_xor_b32_e32 v62, 0x80000000, v40
	v_xor_b32_e32 v61, 0x80000000, v41
	v_xor_b32_e32 v60, 0x80000000, v38
	v_xor_b32_e32 v59, 0x80000000, v39
	v_xor_b32_e32 v58, 0x80000000, v36
	v_xor_b32_e32 v57, 0x80000000, v37
	v_xor_b32_e32 v56, 0x80000000, v34
	v_xor_b32_e32 v55, 0x80000000, v35
	v_xor_b32_e32 v54, 0x80000000, v32
	v_xor_b32_e32 v53, 0x80000000, v33
	v_add_u32_e32 v186, v5, v0
	v_xor_b32_e32 v52, 0x80000000, v46
	v_xor_b32_e32 v51, 0x80000000, v47
	v_xor_b32_e32 v50, 0x80000000, v42
	v_xor_b32_e32 v49, 0x80000000, v45
	v_xor_b32_e32 v48, 0x80000000, v44
	v_mov_b32_e32 v0, v131
	v_mov_b32_e32 v1, v131
	v_mov_b32_e32 v2, v131
	v_mov_b32_e32 v4, v131
	v_mov_b32_e32 v5, v131
	v_mov_b32_e32 v6, v131
	v_mov_b32_e32 v7, v131
	v_mov_b32_e32 v8, v131
	v_mov_b32_e32 v9, v131
	v_mov_b32_e32 v10, v131
	v_mov_b32_e32 v11, v131
	v_mov_b32_e32 v12, v131
	v_mov_b32_e32 v13, v131
	v_mov_b32_e32 v14, v131
	v_mov_b32_e32 v15, v131
	v_mov_b32_e32 v16, v131
	v_mov_b32_e32 v17, v131
	v_mov_b32_e32 v18, v131
	v_mov_b32_e32 v19, v131
	v_mov_b32_e32 v20, v131
	v_mov_b32_e32 v21, v131
	v_mov_b32_e32 v22, v131
	v_mov_b32_e32 v23, v131
	v_mov_b32_e32 v24, v131
	v_mov_b32_e32 v25, v131
	v_mov_b32_e32 v26, v131
	v_mov_b32_e32 v27, v131
	v_mov_b32_e32 v28, v131
	v_mov_b32_e32 v29, v131
	v_mov_b32_e32 v30, v131
	v_mov_b32_e32 v31, v131
	v_add_u32_e32 v131, 0x800, v187
	v_or_b32_e32 v132, 0x80, v130
	v_or_b32_e32 v136, 0x2080, v130
	v_or_b32_e32 v140, 0x4080, v130
	v_or_b32_e32 v144, 0x6080, v130
	v_or_b32_e32 v148, 0x10080, v130
	v_or_b32_e32 v152, 0x12080, v130
	v_or_b32_e32 v156, 0x14080, v130
	v_or_b32_e32 v160, 0x16080, v130
	v_or_b32_e32 v162, 0x20000, v130
	v_or_b32_e32 v158, 0x22000, v130
	v_or_b32_e32 v154, 0x24000, v130
	v_or_b32_e32 v150, 0x26000, v130
	v_or_b32_e32 v146, 0x30000, v130
	v_or_b32_e32 v142, 0x32000, v130
	v_or_b32_e32 v138, 0x34000, v130
	v_or_b32_e32 v134, 0x36000, v130
	s_add_u32 s8, s8, 0x2000
	s_addc_u32 s9, s9, 0
	s_add_u32 s0, s0, 0x2000
	s_addc_u32 s1, s1, 0
	v_add_u32_e32 v204, 0x1000, v128
	s_waitcnt lgkmcnt(0)
	s_barrier
.LBB4_11:
	s_and_b32 s14, s15, 1
	global_load_dwordx4 v[112:115], v128, s[8:9]
	global_load_dwordx4 v[116:119], v204, s[8:9]
	global_load_dwordx4 v[120:123], v128, s[0:1]
	global_load_dwordx4 v[124:127], v204, s[0:1]
	s_add_i32 s15, s15, 1
	s_mul_i32 s18, s14, 0x2400
	v_add_u32_e32 v202, s18, v167
	ds_read_b128 v[80:83], v202
	ds_read_b128 v[190:193], v202 offset:32
	ds_read_b128 v[194:197], v202 offset:4608
	ds_read_b128 v[198:201], v202 offset:4640
	s_waitcnt lgkmcnt(3)
	v_mfma_f32_32x32x16_f16 v[64:79], v[108:111], v[80:83], v[48:63]
	s_waitcnt lgkmcnt(1)
	v_mfma_f32_32x32x16_f16 v[80:95], v[108:111], v[194:197], v[48:63]
	v_mfma_f32_32x32x16_f16 v[64:79], v[104:107], v[190:193], v[64:79]
	ds_read_b128 v[190:193], v202 offset:64
	ds_read_b128 v[194:197], v202 offset:96
	s_waitcnt lgkmcnt(2)
	v_mfma_f32_32x32x16_f16 v[80:95], v[104:107], v[198:201], v[80:95]
	s_waitcnt lgkmcnt(1)
	v_mfma_f32_32x32x16_f16 v[64:79], v[100:103], v[190:193], v[64:79]
	ds_read_b128 v[190:193], v202 offset:4672
	ds_read_b128 v[198:201], v202 offset:4704
	s_waitcnt lgkmcnt(1)
	v_mfma_f32_32x32x16_f16 v[80:95], v[100:103], v[190:193], v[80:95]
	v_mfma_f32_32x32x16_f16 v[64:79], v[96:99], v[194:197], v[64:79]
	s_waitcnt lgkmcnt(0)
	v_mfma_f32_32x32x16_f16 v[80:95], v[96:99], v[198:201], v[80:95]
	s_setprio 2
	s_nop 8
	v_exp_f32_e32 v192, v64
	s_nop 0
	v_exp_f32_e32 v80, v80
	v_exp_f32_e32 v193, v65
	v_exp_f32_e32 v81, v81
	v_mul_f32_e32 v64, v192, v183
	v_exp_f32_e32 v66, v66
	global_store_dword v132, v64, s[42:43] offset:-128
	v_mul_f32_e32 v64, v80, v183
	v_exp_f32_e32 v82, v82
	global_store_dword v132, v64, s[42:43]
	v_mul_f32_e32 v190, v193, v182
	v_exp_f32_e32 v67, v67
	global_store_dword v136, v190, s[42:43] offset:-128
	v_mul_f32_e32 v190, v81, v182
	v_exp_f32_e32 v83, v83
	global_store_dword v136, v190, s[42:43]
	v_mul_f32_e32 v190, v66, v181
	global_store_dword v140, v190, s[42:43] offset:-128
	v_mul_f32_e32 v190, v82, v181
	global_store_dword v140, v190, s[42:43]
	v_mul_f32_e32 v190, v67, v180
	global_store_dword v144, v190, s[42:43] offset:-128
	v_mul_f32_e32 v190, v83, v180
	global_store_dword v144, v190, s[42:43]
	v_exp_f32_e32 v190, v68
	v_cvt_pk_f16_f32 v65, v66, v67
	v_cvt_pk_f16_f32 v67, v82, v83
	v_exp_f32_e32 v82, v84
	v_cvt_pk_f16_f32 v66, v80, v81
	v_mul_f32_e32 v68, v190, v179
	global_store_dword v148, v68, s[42:43] offset:-128
	v_exp_f32_e32 v83, v69
	v_mul_f32_e32 v68, v82, v179
	global_store_dword v148, v68, s[42:43]
	v_exp_f32_e32 v80, v85
	v_mul_f32_e32 v81, v83, v178
	global_store_dword v152, v81, s[42:43] offset:-128
	v_exp_f32_e32 v70, v70
	v_mul_f32_e32 v81, v80, v178
	global_store_dword v152, v81, s[42:43]
	v_exp_f32_e32 v81, v86
	v_mul_f32_e32 v84, v70, v177
	global_store_dword v156, v84, s[42:43] offset:-128
	v_exp_f32_e32 v71, v71
	v_mul_f32_e32 v84, v81, v177
	global_store_dword v156, v84, s[42:43]
	v_exp_f32_e32 v84, v87
	v_mul_f32_e32 v85, v71, v176
	global_store_dword v160, v85, s[42:43] offset:-128
	v_mul_f32_e32 v85, v84, v176
	v_cvt_pk_f16_f32 v64, v192, v193
	global_store_dword v160, v85, s[42:43]
	v_cvt_pk_f16_f32 v69, v70, v71
	v_cvt_pk_f16_f32 v68, v190, v83
	v_exp_f32_e32 v72, v72
	v_cvt_pk_f16_f32 v71, v81, v84
	v_cvt_pk_f16_f32 v70, v82, v80
	ds_write2_b64 v187, v[64:65], v[68:69] offset1:2
	ds_write2_b64 v131, v[66:67], v[70:71] offset0:32 offset1:34
	v_exp_f32_e32 v66, v88
	v_mul_f32_e32 v67, v72, v175
	global_store_dword v162, v67, s[42:43]
	v_exp_f32_e32 v67, v73
	v_mul_f32_e32 v68, v66, v175
	global_store_dword v162, v68, s[42:43] offset:128
	v_exp_f32_e32 v68, v89
	v_mul_f32_e32 v69, v67, v174
	global_store_dword v158, v69, s[42:43]
	v_exp_f32_e32 v69, v74
	v_mul_f32_e32 v70, v68, v174
	global_store_dword v158, v70, s[42:43] offset:128
	v_exp_f32_e32 v70, v90
	v_mul_f32_e32 v71, v69, v173
	global_store_dword v154, v71, s[42:43]
	v_exp_f32_e32 v71, v75
	v_mul_f32_e32 v73, v70, v173
	global_store_dword v154, v73, s[42:43] offset:128
	v_exp_f32_e32 v73, v91
	v_mul_f32_e32 v74, v71, v172
	global_store_dword v150, v74, s[42:43]
	v_mul_f32_e32 v74, v73, v172
	global_store_dword v150, v74, s[42:43] offset:128
	v_cvt_pk_f16_f32 v65, v69, v71
	v_exp_f32_e32 v71, v76
	v_cvt_pk_f16_f32 v64, v72, v67
	v_cvt_pk_f16_f32 v67, v70, v73
	v_exp_f32_e32 v70, v92
	v_cvt_pk_f16_f32 v66, v66, v68
	v_mul_f32_e32 v72, v71, v171
	global_store_dword v146, v72, s[42:43]
	v_exp_f32_e32 v72, v77
	v_mul_f32_e32 v73, v70, v171
	global_store_dword v146, v73, s[42:43] offset:128
	v_exp_f32_e32 v73, v93
	v_mul_f32_e32 v74, v72, v170
	global_store_dword v142, v74, s[42:43]
	v_exp_f32_e32 v74, v78
	v_mul_f32_e32 v75, v73, v170
	global_store_dword v142, v75, s[42:43] offset:128
	v_exp_f32_e32 v75, v94
	v_mul_f32_e32 v76, v74, v169
	global_store_dword v138, v76, s[42:43]
	v_exp_f32_e32 v76, v79
	v_mul_f32_e32 v77, v75, v169
	global_store_dword v138, v77, s[42:43] offset:128
	v_exp_f32_e32 v77, v95
	v_mul_f32_e32 v78, v76, v168
	global_store_dword v134, v78, s[42:43]
	v_mul_f32_e32 v78, v77, v168
	global_store_dword v134, v78, s[42:43] offset:128
	v_cvt_pk_f16_f32 v69, v74, v76
	v_cvt_pk_f16_f32 v68, v71, v72
	v_cvt_pk_f16_f32 v71, v75, v77
	v_cvt_pk_f16_f32 v70, v70, v73
	ds_write2_b64 v187, v[64:65], v[68:69] offset0:4 offset1:6
	ds_write2_b64 v131, v[66:67], v[70:71] offset0:36 offset1:38
	s_setprio 0
	ds_read_b64_tr_b16 v[64:65], v186
	ds_read_b64_tr_b16 v[66:67], v186 offset:288
	s_mul_i32 s18, s14, 0x3000
	v_or_b32_e32 v80, s18, v185
	ds_read_b64_tr_b16 v[68:69], v80
	ds_read_b64_tr_b16 v[70:71], v80 offset:768
	ds_read_b64_tr_b16 v[74:75], v80 offset:832
	ds_read_b64_tr_b16 v[72:73], v80 offset:64
	ds_read_b64_tr_b16 v[76:77], v186 offset:1152
	ds_read_b64_tr_b16 v[78:79], v186 offset:1440
	s_waitcnt lgkmcnt(4)
	v_mfma_f32_32x32x16_f16 v[0:15], v[64:67], v[68:71], v[0:15]
	s_waitcnt lgkmcnt(2)
	v_mfma_f32_32x32x16_f16 v[16:31], v[64:67], v[72:75], v[16:31]
	ds_read_b64_tr_b16 v[64:65], v80 offset:3072
	ds_read_b64_tr_b16 v[66:67], v80 offset:3840
	ds_read_b64_tr_b16 v[70:71], v80 offset:3904
	ds_read_b64_tr_b16 v[68:69], v80 offset:3136
	s_waitcnt lgkmcnt(2)
	v_mfma_f32_32x32x16_f16 v[0:15], v[76:79], v[64:67], v[0:15]
	s_waitcnt lgkmcnt(0)
	v_mfma_f32_32x32x16_f16 v[16:31], v[76:79], v[68:71], v[16:31]
	ds_read_b64_tr_b16 v[64:65], v186 offset:2304
	ds_read_b64_tr_b16 v[66:67], v186 offset:2592
	ds_read_b64_tr_b16 v[68:69], v80 offset:6144
	ds_read_b64_tr_b16 v[70:71], v80 offset:6912
	ds_read_b64_tr_b16 v[74:75], v80 offset:6976
	ds_read_b64_tr_b16 v[72:73], v80 offset:6208
	ds_read_b64_tr_b16 v[76:77], v186 offset:3456
	ds_read_b64_tr_b16 v[78:79], v186 offset:3744
	s_waitcnt lgkmcnt(4)
	v_mfma_f32_32x32x16_f16 v[0:15], v[64:67], v[68:71], v[0:15]
	s_waitcnt lgkmcnt(2)
	v_mfma_f32_32x32x16_f16 v[16:31], v[64:67], v[72:75], v[16:31]
	ds_read_b64_tr_b16 v[64:65], v80 offset:9216
	ds_read_b64_tr_b16 v[66:67], v80 offset:9984
	ds_read_b64_tr_b16 v[70:71], v80 offset:10048
	ds_read_b64_tr_b16 v[68:69], v80 offset:9280
	s_waitcnt lgkmcnt(2)
	v_mfma_f32_32x32x16_f16 v[0:15], v[76:79], v[64:67], v[0:15]
	s_waitcnt lgkmcnt(0)
	v_mfma_f32_32x32x16_f16 v[16:31], v[76:79], v[68:71], v[16:31]
	s_xor_b32 s14, s14, 1
	s_mul_i32 s18, s14, 0x3000
	s_mulk_i32 s14, 0x2400
	s_addk_i32 s14, 0x6000
	s_add_u32 s10, s10, 0x100
	s_addc_u32 s11, s11, 0
	s_add_u32 s42, s42, 0x100
	s_addc_u32 s43, s43, 0
	s_add_u32 s8, s8, 0x2000
	s_addc_u32 s9, s9, 0
	s_add_u32 s0, s0, 0x2000
	s_addc_u32 s1, s1, 0
	v_lshl_add_u32 v67, v166, 1, s14
	s_cmpk_eq_i32 s10, 0x1f00
	v_lshl_add_u32 v64, v189, 1, s18
	v_lshl_add_u32 v65, v188, 1, s18
	v_lshl_add_u32 v66, v165, 1, s14
	s_waitcnt vmcnt(35)
	ds_write_b128 v67, v[112:115]
	s_waitcnt vmcnt(34)
	ds_write_b128 v66, v[116:119]
	s_waitcnt vmcnt(33)
	ds_write_b128 v65, v[120:123]
	s_waitcnt vmcnt(32)
	ds_write_b128 v64, v[124:127]
	s_waitcnt lgkmcnt(0)
	s_barrier
	s_cbranch_scc0 .LBB4_11
	s_lshl_b64 s[0:1], s[16:17], 13
	s_add_u32 s0, s4, s0
	s_addc_u32 s1, s5, s1
	v_xor_b32_e32 v52, 0x80000000, v34
	v_xor_b32_e32 v51, 0x80000000, v35
	v_xor_b32_e32 v50, 0x80000000, v32
	v_xor_b32_e32 v49, 0x80000000, v33
	ds_read_b128 v[32:35], v167 offset:9216
	v_xor_b32_e32 v59, 0x80000000, v43
	v_xor_b32_e32 v58, 0x80000000, v40
	v_xor_b32_e32 v57, 0x80000000, v41
	v_xor_b32_e32 v56, 0x80000000, v38
	v_xor_b32_e32 v55, 0x80000000, v39
	v_xor_b32_e32 v54, 0x80000000, v36
	v_xor_b32_e32 v53, 0x80000000, v37
	v_xor_b32_e32 v48, 0x80000000, v46
	v_xor_b32_e32 v47, 0x80000000, v47
	v_xor_b32_e32 v46, 0x80000000, v42
	v_xor_b32_e32 v45, 0x80000000, v45
	v_xor_b32_e32 v44, 0x80000000, v44
	ds_read_b128 v[36:39], v167 offset:9248
	s_add_u32 s0, s0, 0x1f00
	s_waitcnt lgkmcnt(1)
	v_mfma_f32_32x32x16_f16 v[60:75], v[108:111], v[32:35], v[44:59]
	ds_read_b128 v[32:35], v167 offset:13824
	ds_read_b128 v[40:43], v167 offset:13856
	s_addc_u32 s1, s1, 0
	s_waitcnt lgkmcnt(1)
	v_mfma_f32_32x32x16_f16 v[44:59], v[108:111], v[32:35], v[44:59]
	v_mfma_f32_32x32x16_f16 v[60:75], v[104:107], v[36:39], v[60:75]
	ds_read_b128 v[32:35], v167 offset:9280
	ds_read_b128 v[36:39], v167 offset:9312
	s_waitcnt lgkmcnt(2)
	v_mfma_f32_32x32x16_f16 v[44:59], v[104:107], v[40:43], v[44:59]
	s_waitcnt lgkmcnt(1)
	v_mfma_f32_32x32x16_f16 v[60:75], v[100:103], v[32:35], v[60:75]
	ds_read_b128 v[32:35], v167 offset:13888
	ds_read_b128 v[40:43], v167 offset:13920
	s_waitcnt lgkmcnt(1)
	v_mfma_f32_32x32x16_f16 v[44:59], v[100:103], v[32:35], v[44:59]
	v_mfma_f32_32x32x16_f16 v[60:75], v[96:99], v[36:39], v[60:75]
	s_waitcnt lgkmcnt(0)
	v_mfma_f32_32x32x16_f16 v[44:59], v[96:99], v[40:43], v[44:59]
	s_setprio 2
	s_nop 8
	v_exp_f32_e32 v32, v60
	s_nop 0
	v_exp_f32_e32 v34, v44
	v_exp_f32_e32 v35, v61
	v_or_b32_e32 v37, 0x2000, v130
	v_mul_f32_e32 v33, v32, v183
	v_mul_f32_e32 v36, v34, v183
	global_store_dword v130, v33, s[0:1]
	global_store_dword v130, v36, s[0:1] offset:128
	v_exp_f32_e32 v36, v45
	v_mul_f32_e32 v33, v35, v182
	global_store_dword v37, v33, s[0:1]
	v_exp_f32_e32 v33, v62
	v_mul_f32_e32 v38, v36, v182
	global_store_dword v37, v38, s[0:1] offset:128
	v_exp_f32_e32 v37, v46
	v_mul_f32_e32 v38, v33, v181
	v_or_b32_e32 v39, 0x4000, v130
	global_store_dword v39, v38, s[0:1]
	v_exp_f32_e32 v38, v63
	v_mul_f32_e32 v40, v37, v181
	global_store_dword v39, v40, s[0:1] offset:128
	v_exp_f32_e32 v39, v47
	v_mul_f32_e32 v40, v38, v180
	v_cvt_pk_f16_f32 v33, v33, v38
	v_exp_f32_e32 v38, v64
	v_or_b32_e32 v41, 0x6000, v130
	global_store_dword v41, v40, s[0:1]
	v_mul_f32_e32 v40, v39, v180
	global_store_dword v41, v40, s[0:1] offset:128
	v_cvt_pk_f16_f32 v32, v32, v35
	v_cvt_pk_f16_f32 v35, v37, v39
	v_cvt_pk_f16_f32 v34, v34, v36
	v_exp_f32_e32 v40, v48
	v_mul_f32_e32 v36, v38, v179
	v_or_b32_e32 v37, 0x10000, v130
	global_store_dword v37, v36, s[0:1]
	v_exp_f32_e32 v36, v65
	v_exp_f32_e32 v41, v49
	v_mul_f32_e32 v39, v40, v179
	global_store_dword v37, v39, s[0:1] offset:128
	v_mul_f32_e32 v37, v36, v178
	v_or_b32_e32 v39, 0x12000, v130
	global_store_dword v39, v37, s[0:1]
	v_exp_f32_e32 v37, v66
	v_mul_f32_e32 v42, v41, v178
	global_store_dword v39, v42, s[0:1] offset:128
	v_exp_f32_e32 v39, v50
	v_mul_f32_e32 v42, v37, v177
	v_or_b32_e32 v43, 0x14000, v130
	global_store_dword v43, v42, s[0:1]
	v_exp_f32_e32 v42, v67
	v_mul_f32_e32 v44, v39, v177
	global_store_dword v43, v44, s[0:1] offset:128
	v_exp_f32_e32 v43, v51
	v_cvt_pk_f16_f32 v37, v37, v42
	v_cvt_pk_f16_f32 v36, v38, v36
	v_cvt_pk_f16_f32 v38, v40, v41
	v_cvt_pk_f16_f32 v39, v39, v43
	ds_write2_b64 v187, v[32:33], v[36:37] offset1:2
	v_exp_f32_e32 v32, v68
	v_add_u32_e32 v40, 0x800, v187
	ds_write2_b64 v40, v[34:35], v[38:39] offset0:32 offset1:34
	v_exp_f32_e32 v34, v52
	v_exp_f32_e32 v36, v69
	v_exp_f32_e32 v37, v53
	v_mul_f32_e32 v33, v32, v175
	v_or_b32_e32 v35, 0x20000, v130
	global_store_dword v35, v33, s[0:1]
	v_mul_f32_e32 v33, v34, v175
	global_store_dword v35, v33, s[0:1] offset:128
	v_mul_f32_e32 v33, v36, v174
	v_or_b32_e32 v35, 0x22000, v130
	global_store_dword v35, v33, s[0:1]
	v_exp_f32_e32 v33, v70
	v_mul_f32_e32 v38, v37, v174
	global_store_dword v35, v38, s[0:1] offset:128
	v_exp_f32_e32 v35, v54
	v_mul_f32_e32 v38, v33, v173
	v_or_b32_e32 v39, 0x24000, v130
	global_store_dword v39, v38, s[0:1]
	v_exp_f32_e32 v38, v71
	v_mul_f32_e32 v41, v35, v173
	global_store_dword v39, v41, s[0:1] offset:128
	v_exp_f32_e32 v39, v55
	v_mul_f32_e32 v44, v42, v176
	v_mul_f32_e32 v41, v38, v172
	v_or_b32_e32 v42, 0x26000, v130
	v_cvt_pk_f16_f32 v32, v32, v36
	v_exp_f32_e32 v36, v72
	global_store_dword v42, v41, s[0:1]
	v_mul_f32_e32 v41, v39, v172
	v_cvt_pk_f16_f32 v33, v33, v38
	v_exp_f32_e32 v38, v56
	global_store_dword v42, v41, s[0:1] offset:128
	v_exp_f32_e32 v41, v73
	v_exp_f32_e32 v42, v57
	v_cvt_pk_f16_f32 v35, v35, v39
	v_cvt_pk_f16_f32 v34, v34, v37
	v_mul_f32_e32 v37, v36, v171
	v_or_b32_e32 v39, 0x30000, v130
	global_store_dword v39, v37, s[0:1]
	v_mul_f32_e32 v37, v38, v171
	v_or_b32_e32 v45, 0x16000, v130
	global_store_dword v39, v37, s[0:1] offset:128
	v_mul_f32_e32 v37, v41, v170
	v_or_b32_e32 v39, 0x32000, v130
	global_store_dword v45, v44, s[0:1]
	v_mul_f32_e32 v44, v43, v176
	global_store_dword v39, v37, s[0:1]
	v_exp_f32_e32 v37, v74
	v_mul_f32_e32 v43, v42, v170
	global_store_dword v39, v43, s[0:1] offset:128
	v_exp_f32_e32 v39, v58
	global_store_dword v45, v44, s[0:1] offset:128
	v_mul_f32_e32 v43, v37, v169
	v_or_b32_e32 v44, 0x34000, v130
	global_store_dword v44, v43, s[0:1]
	v_exp_f32_e32 v43, v75
	v_mul_f32_e32 v45, v39, v169
	global_store_dword v44, v45, s[0:1] offset:128
	v_exp_f32_e32 v44, v59
	v_mul_f32_e32 v45, v43, v168
	v_or_b32_e32 v46, 0x36000, v130
	global_store_dword v46, v45, s[0:1]
	v_mul_f32_e32 v45, v44, v168
	v_cvt_pk_f16_f32 v37, v37, v43
	v_cvt_pk_f16_f32 v36, v36, v41
	global_store_dword v46, v45, s[0:1] offset:128
	v_cvt_pk_f16_f32 v39, v39, v44
	v_cvt_pk_f16_f32 v38, v38, v42
	ds_write2_b64 v187, v[32:33], v[36:37] offset0:4 offset1:6
	ds_write2_b64 v40, v[34:35], v[38:39] offset0:36 offset1:38
	s_setprio 0
	ds_read_b64_tr_b16 v[32:33], v186
	ds_read_b64_tr_b16 v[34:35], v186 offset:288
	ds_read_b64_tr_b16 v[36:37], v185 offset:12288
	ds_read_b64_tr_b16 v[38:39], v185 offset:13056
	ds_read_b64_tr_b16 v[42:43], v185 offset:13120
	ds_read_b64_tr_b16 v[40:41], v185 offset:12352
	ds_read_b64_tr_b16 v[44:45], v186 offset:1152
	ds_read_b64_tr_b16 v[46:47], v186 offset:1440
	s_waitcnt lgkmcnt(4)
	v_mfma_f32_32x32x16_f16 v[0:15], v[32:35], v[36:39], v[0:15]
	s_waitcnt lgkmcnt(2)
	v_mfma_f32_32x32x16_f16 v[16:31], v[32:35], v[40:43], v[16:31]
	ds_read_b64_tr_b16 v[32:33], v185 offset:15360
	ds_read_b64_tr_b16 v[34:35], v185 offset:16128
	ds_read_b64_tr_b16 v[38:39], v185 offset:16192
	ds_read_b64_tr_b16 v[36:37], v185 offset:15424
	s_waitcnt lgkmcnt(2)
	v_mfma_f32_32x32x16_f16 v[0:15], v[44:47], v[32:35], v[0:15]
	s_waitcnt lgkmcnt(0)
	v_mfma_f32_32x32x16_f16 v[16:31], v[44:47], v[36:39], v[16:31]
	ds_read_b64_tr_b16 v[32:33], v186 offset:2304
	ds_read_b64_tr_b16 v[34:35], v186 offset:2592
	ds_read_b64_tr_b16 v[36:37], v185 offset:18432
	ds_read_b64_tr_b16 v[38:39], v185 offset:19200
	ds_read_b64_tr_b16 v[42:43], v185 offset:19264
	ds_read_b64_tr_b16 v[40:41], v185 offset:18496
	ds_read_b64_tr_b16 v[44:45], v186 offset:3456
	ds_read_b64_tr_b16 v[46:47], v186 offset:3744
	s_waitcnt lgkmcnt(4)
	v_mfma_f32_32x32x16_f16 v[0:15], v[32:35], v[36:39], v[0:15]
	s_waitcnt lgkmcnt(2)
	v_mfma_f32_32x32x16_f16 v[16:31], v[32:35], v[40:43], v[16:31]
	ds_read_b64_tr_b16 v[32:33], v185 offset:21504
	ds_read_b64_tr_b16 v[34:35], v185 offset:22272
	ds_read_b64_tr_b16 v[38:39], v185 offset:22336
	ds_read_b64_tr_b16 v[36:37], v185 offset:21568
	s_waitcnt lgkmcnt(2)
	v_mfma_f32_32x32x16_f16 v[0:15], v[44:47], v[32:35], v[0:15]
	s_waitcnt lgkmcnt(0)
	v_mfma_f32_32x32x16_f16 v[16:31], v[44:47], v[36:39], v[16:31]
	s_lshl_b32 s0, s2, 3
	s_and_b32 s0, s0, 0x7ffff800
	s_add_i32 s3, s3, s0
	s_lshl_b32 s0, s12, 7
	s_and_b32 s0, s0, 0x780
	s_add_u32 s0, s6, s0
	v_mov_b32_e32 v35, 0
	v_or_b32_e32 v32, s3, v184
	s_addc_u32 s1, s7, 0
	v_lshlrev_b32_e32 v34, 1, v164
	v_mov_b32_e32 v33, v35
	v_lshl_add_u64 v[36:37], s[0:1], 0, v[34:35]
	v_lshlrev_b64 v[38:39], 11, v[32:33]
	v_fma_mixlo_f16 v0, v0, v183, 0
	v_lshl_add_u64 v[38:39], v[36:37], 0, v[38:39]
	s_waitcnt vmcnt(63) expcnt(7) lgkmcnt(15)
	s_barrier
	global_store_short v[38:39], v0, off
	v_fma_mixlo_f16 v0, v16, v183, 0
	v_or_b32_e32 v34, 1, v32
	global_store_short v[38:39], v0, off offset:64
	v_lshlrev_b64 v[38:39], 11, v[34:35]
	v_fma_mixlo_f16 v16, v1, v182, 0
	v_lshl_add_u64 v[0:1], v[36:37], 0, v[38:39]
	global_store_short v[0:1], v16, off
	v_fma_mixlo_f16 v16, v17, v182, 0
	v_or_b32_e32 v34, 2, v32
	global_store_short v[0:1], v16, off offset:64
	v_lshlrev_b64 v[0:1], 11, v[34:35]
	v_fma_mixlo_f16 v2, v2, v181, 0
	v_lshl_add_u64 v[0:1], v[36:37], 0, v[0:1]
	global_store_short v[0:1], v2, off
	v_fma_mixlo_f16 v2, v18, v181, 0
	v_or_b32_e32 v34, 3, v32
	global_store_short v[0:1], v2, off offset:64
	v_lshlrev_b64 v[0:1], 11, v[34:35]
	v_fma_mixlo_f16 v2, v3, v180, 0
	v_lshl_add_u64 v[0:1], v[36:37], 0, v[0:1]
	global_store_short v[0:1], v2, off
	v_fma_mixlo_f16 v2, v19, v180, 0
	v_or_b32_e32 v34, 8, v32
	global_store_short v[0:1], v2, off offset:64
	v_lshlrev_b64 v[0:1], 11, v[34:35]
	v_fma_mixlo_f16 v2, v4, v179, 0
	v_lshl_add_u64 v[0:1], v[36:37], 0, v[0:1]
	global_store_short v[0:1], v2, off
	v_fma_mixlo_f16 v2, v20, v179, 0
	v_or_b32_e32 v34, 9, v32
	global_store_short v[0:1], v2, off offset:64
	v_lshlrev_b64 v[0:1], 11, v[34:35]
	v_fma_mixlo_f16 v2, v5, v178, 0
	v_lshl_add_u64 v[0:1], v[36:37], 0, v[0:1]
	global_store_short v[0:1], v2, off
	v_fma_mixlo_f16 v2, v21, v178, 0
	v_or_b32_e32 v34, 10, v32
	global_store_short v[0:1], v2, off offset:64
	v_lshlrev_b64 v[0:1], 11, v[34:35]
	v_fma_mixlo_f16 v2, v6, v177, 0
	v_lshl_add_u64 v[0:1], v[36:37], 0, v[0:1]
	global_store_short v[0:1], v2, off
	v_fma_mixlo_f16 v2, v22, v177, 0
	v_or_b32_e32 v34, 11, v32
	global_store_short v[0:1], v2, off offset:64
	v_lshlrev_b64 v[0:1], 11, v[34:35]
	v_fma_mixlo_f16 v2, v7, v176, 0
	v_lshl_add_u64 v[0:1], v[36:37], 0, v[0:1]
	global_store_short v[0:1], v2, off
	v_fma_mixlo_f16 v2, v23, v176, 0
	v_or_b32_e32 v34, 16, v32
	global_store_short v[0:1], v2, off offset:64
	v_lshlrev_b64 v[0:1], 11, v[34:35]
	v_fma_mixlo_f16 v2, v8, v175, 0
	v_lshl_add_u64 v[0:1], v[36:37], 0, v[0:1]
	global_store_short v[0:1], v2, off
	v_fma_mixlo_f16 v2, v24, v175, 0
	v_or_b32_e32 v34, 17, v32
	global_store_short v[0:1], v2, off offset:64
	v_lshlrev_b64 v[0:1], 11, v[34:35]
	v_fma_mixlo_f16 v2, v9, v174, 0
	v_lshl_add_u64 v[0:1], v[36:37], 0, v[0:1]
	global_store_short v[0:1], v2, off
	v_fma_mixlo_f16 v2, v25, v174, 0
	v_or_b32_e32 v34, 18, v32
	global_store_short v[0:1], v2, off offset:64
	v_lshlrev_b64 v[0:1], 11, v[34:35]
	v_fma_mixlo_f16 v2, v10, v173, 0
	v_lshl_add_u64 v[0:1], v[36:37], 0, v[0:1]
	global_store_short v[0:1], v2, off
	v_fma_mixlo_f16 v2, v26, v173, 0
	v_or_b32_e32 v34, 19, v32
	global_store_short v[0:1], v2, off offset:64
	v_lshlrev_b64 v[0:1], 11, v[34:35]
	v_fma_mixlo_f16 v2, v11, v172, 0
	v_lshl_add_u64 v[0:1], v[36:37], 0, v[0:1]
	global_store_short v[0:1], v2, off
	v_fma_mixlo_f16 v2, v27, v172, 0
	v_or_b32_e32 v34, 24, v32
	global_store_short v[0:1], v2, off offset:64
	v_lshlrev_b64 v[0:1], 11, v[34:35]
	v_fma_mixlo_f16 v2, v12, v171, 0
	v_lshl_add_u64 v[0:1], v[36:37], 0, v[0:1]
	global_store_short v[0:1], v2, off
	v_fma_mixlo_f16 v2, v28, v171, 0
	v_or_b32_e32 v34, 25, v32
	global_store_short v[0:1], v2, off offset:64
	v_lshlrev_b64 v[0:1], 11, v[34:35]
	v_fma_mixlo_f16 v2, v13, v170, 0
	v_lshl_add_u64 v[0:1], v[36:37], 0, v[0:1]
	global_store_short v[0:1], v2, off
	v_fma_mixlo_f16 v2, v29, v170, 0
	v_or_b32_e32 v34, 26, v32
	global_store_short v[0:1], v2, off offset:64
	v_lshlrev_b64 v[0:1], 11, v[34:35]
	v_fma_mixlo_f16 v2, v14, v169, 0
	v_lshl_add_u64 v[0:1], v[36:37], 0, v[0:1]
	global_store_short v[0:1], v2, off
	v_fma_mixlo_f16 v2, v30, v169, 0
	v_or_b32_e32 v34, 27, v32
	global_store_short v[0:1], v2, off offset:64
	v_lshlrev_b64 v[0:1], 11, v[34:35]
	v_fma_mixlo_f16 v2, v15, v168, 0
	v_lshl_add_u64 v[0:1], v[36:37], 0, v[0:1]
	global_store_short v[0:1], v2, off
	v_fma_mixlo_f16 v2, v31, v168, 0
	global_store_short v[0:1], v2, off offset:64
	s_endpgm
	.p2alignl 8, 3212836864
